# baseline (speedup 1.0000x reference)
.LBB1_17:
	s_bitcmp0_b32 s3, 7
	s_mov_b32 s27, 0x8000
	s_cselect_b32 s3, s27, 0x18000
	s_add_i32 s3, s3, 0
	s_lshl_b32 s6, s18, 13
	s_add_i32 s3, s3, s6
	v_add_u32_e32 v199, s3, v209
	s_nop 2
	v_cvt_pk_bf16_f32 v0, v0, v1
	v_cvt_pk_bf16_f32 v1, v2, v3
	v_cvt_pk_bf16_f32 v2, v4, v5
	v_cvt_pk_bf16_f32 v3, v6, v7
	s_lshl_b64 s[6:7], s[10:11], 20
	s_mov_b32 s17, 0
	ds_write_b128 v199, v[0:3] offset:6144
	v_cvt_pk_bf16_f32 v0, v8, v9
	v_cvt_pk_bf16_f32 v1, v10, v11
	v_cvt_pk_bf16_f32 v2, v12, v13
	v_cvt_pk_bf16_f32 v3, v14, v15
	s_mov_b32 s16, s4
	ds_write_b128 v199, v[0:3] offset:7168
	v_cvt_pk_bf16_f32 v0, v16, v17
	v_cvt_pk_bf16_f32 v1, v18, v19
	v_cvt_pk_bf16_f32 v2, v20, v21
	v_cvt_pk_bf16_f32 v3, v22, v23
	s_lshl_b64 s[14:15], s[16:17], 12
	ds_write_b128 v199, v[0:3] offset:22528
	v_cvt_pk_bf16_f32 v0, v24, v25
	v_cvt_pk_bf16_f32 v1, v26, v27
	v_cvt_pk_bf16_f32 v2, v28, v29
	v_cvt_pk_bf16_f32 v3, v30, v31
	ds_write_b128 v199, v[0:3] offset:23552
	s_mov_b32 s3, s17
	v_cvt_pk_bf16_f32 v48, v48, v49
	v_cvt_pk_bf16_f32 v49, v50, v51
	v_cvt_pk_bf16_f32 v50, v52, v53
	v_cvt_pk_bf16_f32 v51, v54, v55
	ds_write_b128 v199, v[48:51] offset:4096
	v_cvt_pk_bf16_f32 v50, v60, v61
	v_cvt_pk_bf16_f32 v51, v62, v63
	v_cvt_pk_bf16_f32 v64, v64, v65
	v_cvt_pk_bf16_f32 v65, v66, v67
	v_cvt_pk_bf16_f32 v66, v68, v69
	v_cvt_pk_bf16_f32 v67, v70, v71
	ds_write_b128 v199, v[64:67] offset:18432
	v_cvt_pk_bf16_f32 v66, v76, v77
	v_cvt_pk_bf16_f32 v67, v78, v79
	v_cvt_pk_bf16_f32 v64, v72, v73
	v_cvt_pk_bf16_f32 v65, v74, v75
	ds_write_b128 v199, v[64:67] offset:19456
	v_cvt_pk_bf16_f32 v48, v56, v57
	v_cvt_pk_bf16_f32 v49, v58, v59
	ds_write_b128 v199, v[48:51] offset:5120
	v_cvt_pk_bf16_f32 v80, v80, v81
	v_cvt_pk_bf16_f32 v81, v82, v83
	v_cvt_pk_bf16_f32 v82, v84, v85
	v_cvt_pk_bf16_f32 v83, v86, v87
	ds_write_b128 v199, v[80:83] offset:2048
	v_cvt_pk_bf16_f32 v80, v88, v89
	v_cvt_pk_bf16_f32 v81, v90, v91
	v_cvt_pk_bf16_f32 v82, v92, v93
	v_cvt_pk_bf16_f32 v83, v94, v95
	ds_write_b128 v199, v[80:83] offset:3072
	v_cvt_pk_bf16_f32 v32, v32, v33
	v_cvt_pk_bf16_f32 v33, v34, v35
	v_cvt_pk_bf16_f32 v34, v36, v37
	v_cvt_pk_bf16_f32 v35, v38, v39
	ds_write_b128 v199, v[32:35] offset:20480
	v_cvt_pk_bf16_f32 v32, v40, v41
	v_cvt_pk_bf16_f32 v33, v42, v43
	v_cvt_pk_bf16_f32 v34, v44, v45
	v_cvt_pk_bf16_f32 v35, v46, v47
	ds_write_b128 v199, v[32:35] offset:21504
	v_cvt_pk_bf16_f32 v112, v112, v113
	v_cvt_pk_bf16_f32 v113, v114, v115
	v_cvt_pk_bf16_f32 v114, v116, v117
	v_cvt_pk_bf16_f32 v115, v118, v119
	v_cvt_pk_bf16_f32 v96, v96, v97
	v_cvt_pk_bf16_f32 v97, v98, v99
	v_cvt_pk_bf16_f32 v98, v100, v101
	v_cvt_pk_bf16_f32 v99, v102, v103
	ds_write_b128 v199, v[112:115]
	v_cvt_pk_bf16_f32 v112, v120, v121
	v_cvt_pk_bf16_f32 v113, v122, v123
	v_cvt_pk_bf16_f32 v114, v124, v125
	v_cvt_pk_bf16_f32 v115, v126, v127
	ds_write_b128 v199, v[96:99] offset:16384
	v_cvt_pk_bf16_f32 v96, v104, v105
	v_cvt_pk_bf16_f32 v97, v106, v107
	v_cvt_pk_bf16_f32 v98, v108, v109
	v_cvt_pk_bf16_f32 v99, v110, v111
	ds_write_b128 v199, v[112:115] offset:1024
	ds_write_b128 v199, v[96:99] offset:17408
	s_add_u32 s3, s12, s6
	s_addc_u32 s18, s13, s7
	s_add_u32 s16, s3, s14
	s_addc_u32 s18, s18, s15
	s_lshl_b32 s17, s2, 2
	v_lshlrev_b32_e32 v0, 7, v194
	s_add_u32 s16, s16, s17
	v_and_b32_e32 v0, 0xfffffc00, v0
	s_addc_u32 s17, s18, 0
	v_ashrrev_i32_e32 v1, 31, v0
	v_and_b32_e32 v2, 28, v195
	v_lshl_add_u64 v[0:1], v[0:1], 2, s[16:17]
	v_lshlrev_b32_e32 v2, 2, v2
	v_mov_b32_e32 v3, 0
	v_lshl_add_u64 v[0:1], v[0:1], 0, v[2:3]
	v_add_co_u32_e32 v2, vcc, s27, v0
	v_addc_co_u32_e32 v3, vcc, 0, v1, vcc
	s_mov_b32 s16, 0x10000
	global_load_dwordx4 v[52:55], v[0:1], off nt
	global_load_dwordx4 v[60:63], v[2:3], off nt
	v_add_co_u32_e32 v2, vcc, s16, v0
	s_mov_b32 s19, 0x18000
	v_addc_co_u32_e32 v3, vcc, 0, v1, vcc
	global_load_dwordx4 v[76:79], v[2:3], off nt
	v_add_co_u32_e32 v2, vcc, s19, v0
	v_addc_co_u32_e32 v3, vcc, 0, v1, vcc
	s_mov_b32 s16, 0x40000
	global_load_dwordx4 v[64:67], v[2:3], off nt
	v_add_co_u32_e32 v2, vcc, s16, v0
	s_mov_b32 s16, 0x48000
	s_nop 0
	v_addc_co_u32_e32 v3, vcc, 0, v1, vcc
	global_load_dwordx4 v[68:71], v[2:3], off nt
	v_add_co_u32_e32 v2, vcc, s16, v0
	s_mov_b32 s16, 0x50000
	s_nop 0
	v_addc_co_u32_e32 v3, vcc, 0, v1, vcc
	global_load_dwordx4 v[72:75], v[2:3], off nt
	v_add_co_u32_e32 v2, vcc, s16, v0
	s_mov_b32 s16, 0x58000
	s_nop 0
	v_addc_co_u32_e32 v3, vcc, 0, v1, vcc
	global_load_dwordx4 v[56:59], v[2:3], off nt
	v_add_co_u32_e32 v2, vcc, s16, v0
	s_mov_b32 s16, 0x80000
	s_nop 0
	v_addc_co_u32_e32 v3, vcc, 0, v1, vcc
	global_load_dwordx4 v[48:51], v[2:3], off nt
	v_add_co_u32_e32 v2, vcc, s16, v0
	v_addc_co_u32_e32 v3, vcc, 0, v1, vcc
	s_mov_b32 s16, 0x88000
	global_load_dwordx4 v[88:91], v[2:3], off nt
	v_add_co_u32_e32 v2, vcc, s16, v0
	s_mov_b32 s16, 0x90000
	s_nop 0
	v_addc_co_u32_e32 v3, vcc, 0, v1, vcc
	global_load_dwordx4 v[92:95], v[2:3], off nt
	v_add_co_u32_e32 v2, vcc, s16, v0
	s_mov_b32 s16, 0x98000
	s_nop 0
	v_addc_co_u32_e32 v3, vcc, 0, v1, vcc
	global_load_dwordx4 v[80:83], v[2:3], off nt
	v_add_co_u32_e32 v2, vcc, s16, v0
	s_mov_b32 s16, 0xc0000
	s_nop 0
	v_addc_co_u32_e32 v3, vcc, 0, v1, vcc
	global_load_dwordx4 v[84:87], v[2:3], off nt
	v_add_co_u32_e32 v2, vcc, s16, v0
	v_addc_co_u32_e32 v3, vcc, 0, v1, vcc
	s_mov_b32 s16, 0xc8000
	global_load_dwordx4 v[40:43], v[2:3], off nt
	v_add_co_u32_e32 v2, vcc, s16, v0
	s_nop 0
	v_addc_co_u32_e32 v3, vcc, 0, v1, vcc
	global_load_dwordx4 v[44:47], v[2:3], off nt
	v_add_co_u32_e32 v2, vcc, 0xd0000, v0
	s_nop 0
	v_addc_co_u32_e32 v3, vcc, 0, v1, vcc
	v_add_co_u32_e32 v0, vcc, 0xd8000, v0
	global_load_dwordx4 v[32:35], v[2:3], off nt
	s_nop 0
	v_addc_co_u32_e32 v1, vcc, 0, v1, vcc
	global_load_dwordx4 v[36:39], v[0:1], off nt
	s_mov_b32 s3, 0
	s_load_dwordx2 s[0:1], s[0:1], 0x30
	s_branch .LBB1_24

.LBB1_24:
	s_cmp_lt_u32 s20, 2
	s_mov_b32 s10, 0x8000
	s_cselect_b32 s11, s10, 0x18000
	s_lshl_b32 s12, s22, 14
	s_add_i32 s11, s11, 0
	s_and_b32 s12, s12, 0x4000
	s_add_i32 s11, s11, s12
	s_waitcnt lgkmcnt(0)
	s_barrier
	s_nop 0
	v_lshl_add_u32 v3, v193, 4, s11
	s_lshl_b32 s11, s20, 8
	v_lshlrev_b32_e32 v0, 2, v193
	s_add_i32 s11, s11, 0
	v_and_b32_e32 v1, 12, v0
	v_add_u32_e32 v0, s11, v0
	v_add_u32_e32 v0, 0x20840, v0
	s_add_u32 s12, s8, 0x10000
	ds_read_b128 v[152:155], v3
	ds_read_b128 v[148:151], v3 offset:1024
	ds_read_b128 v[140:143], v3 offset:2048
	ds_read_b128 v[128:131], v3 offset:3072
	ds_read_b128 v[120:123], v3 offset:4096
	ds_read_b128 v[112:115], v3 offset:5120
	ds_read_b128 v[108:111], v3 offset:6144
	ds_read_b128 v[100:103], v3 offset:7168
	ds_read_b128 v[156:159], v3 offset:8192
	ds_read_b128 v[144:147], v3 offset:9216
	ds_read_b128 v[136:139], v3 offset:10240
	ds_read_b128 v[132:135], v3 offset:11264
	ds_read_b128 v[124:127], v3 offset:12288
	ds_read_b128 v[116:119], v3 offset:13312
	ds_read_b128 v[104:107], v3 offset:14336
	ds_read_b128 v[96:99], v3 offset:15360
	s_waitcnt lgkmcnt(0)
	ds_read_b32 v180, v0
	s_waitcnt lgkmcnt(0)
	s_barrier
	v_ashrrev_i32_e32 v164, 5, v193
	v_and_b32_e32 v166, 31, v193
	v_bfe_u32 v2, v193, 2, 2
	v_bitop3_b32 v1, v1, v164, v2 bitop3:0x36
	v_or_b32_e32 v2, s4, v166
	v_lshl_add_u32 v167, v2, 9, 0
	v_lshlrev_b32_e32 v165, 4, v1
	v_add_u32_e32 v181, 0x10000, v167
	v_add_u32_e32 v4, v181, v165
	ds_read_b128 v[0:3], v4
	ds_read_b128 v[4:7], v4 offset:256
	s_waitcnt lgkmcnt(1)
	v_mfma_f32_32x32x16_bf16 v[16:31], v[0:3], v[152:155], 0
	s_addc_u32 s13, s9, 0
	s_mov_b32 s11, m0
	s_mov_b32 m0, s23
	s_nop 0
	global_load_lds_dwordx4 v192, s[12:13]
	s_mov_b32 m0, s11
	s_add_u32 s12, s8, 0x12000
	s_addc_u32 s13, s9, 0
	s_mov_b32 s11, m0
	s_mov_b32 m0, s24
	s_nop 0
	global_load_lds_dwordx4 v192, s[12:13]
	s_mov_b32 m0, s11
	s_add_u32 s12, s8, 0x14000
	s_addc_u32 s13, s9, 0
	s_mov_b32 s11, m0
	s_mov_b32 m0, s25
	s_nop 0
	global_load_lds_dwordx4 v192, s[12:13]
	s_mov_b32 m0, s11
	s_add_u32 s12, s8, 0x16000
	s_addc_u32 s13, s9, 0
	s_mov_b32 s11, m0
	s_mov_b32 m0, s26
	s_nop 0
	global_load_lds_dwordx4 v192, s[12:13]
	s_mov_b32 m0, s11
	s_add_u32 s12, s8, 0x18000
	s_addc_u32 s13, s9, 0
	s_add_i32 s11, s21, 0x18000
	s_mov_b32 s16, m0
	s_mov_b32 m0, s11
	s_nop 0
	global_load_lds_dwordx4 v192, s[12:13]
	s_mov_b32 m0, s16
	s_add_u32 s12, s8, 0x1a000
	s_addc_u32 s13, s9, 0
	s_add_i32 s11, s21, 0x1a000
	s_mov_b32 s16, m0
	s_mov_b32 m0, s11
	s_nop 0
	global_load_lds_dwordx4 v192, s[12:13]
	s_mov_b32 m0, s16
	s_add_u32 s12, s8, 0x1c000
	s_addc_u32 s13, s9, 0
	s_add_i32 s11, s21, 0x1c000
	s_mov_b32 s16, m0
	s_mov_b32 m0, s11
	s_nop 0
	global_load_lds_dwordx4 v192, s[12:13]
	s_mov_b32 m0, s16
	s_add_u32 s8, s8, 0x1e000
	s_addc_u32 s9, s9, 0
	s_add_i32 s11, s21, 0x1e000
	s_mov_b32 s12, m0
	s_mov_b32 m0, s11
	s_nop 0
	global_load_lds_dwordx4 v192, s[8:9]
	s_mov_b32 m0, s12
	v_xor_b32_e32 v170, 32, v165
	v_add_u32_e32 v8, v181, v170
	v_xor_b32_e32 v168, 64, v165
	v_xor_b32_e32 v171, 0x60, v165
	v_xor_b32_e32 v169, 0x80, v165
	v_xor_b32_e32 v172, 0xa0, v165
	v_add_u32_e32 v204, v167, v165
	s_waitcnt lgkmcnt(0)
	v_mfma_f32_32x32x16_bf16 v[16:31], v[4:7], v[156:159], v[16:31]
	ds_read_b128 v[0:3], v8
	ds_read_b128 v[4:7], v8 offset:256
	v_add_u32_e32 v8, v181, v168
	v_xor_b32_e32 v173, 0xc0, v165
	v_add_u32_e32 v207, v167, v168
	s_movk_i32 s8, 0x240
	v_mul_lo_u32 v164, v164, s8
	v_add_u32_e32 v209, v167, v171
	s_waitcnt lgkmcnt(1)
	v_mfma_f32_32x32x16_bf16 v[16:31], v[0:3], v[148:151], v[16:31]
	v_add_u32_e32 v210, v167, v169
	v_ashrrev_i32_e32 v205, 3, v193
	v_and_b32_e32 v206, 7, v193
	s_mulk_i32 s20, 0x1200
	s_movk_i32 s11, 0x90
	v_add_u32_e32 v208, s4, v205
	s_add_i32 s4, s5, 0
	s_waitcnt lgkmcnt(0)
	v_mfma_f32_32x32x16_bf16 v[16:31], v[4:7], v[144:147], v[16:31]
	ds_read_b128 v[0:3], v8
	ds_read_b128 v[4:7], v8 offset:256
	v_add_u32_e32 v8, v181, v171
	v_mul_lo_u32 v184, v205, s11
	v_lshlrev_b32_e32 v185, 4, v206
	s_add_i32 s4, s4, s20
	v_add_u32_e32 v211, v167, v172
	v_add_u32_e32 v212, v167, v173
	s_waitcnt lgkmcnt(1)
	v_mfma_f32_32x32x16_bf16 v[16:31], v[0:3], v[140:143], v[16:31]
	v_lshlrev_b32_e32 v166, 2, v166
	v_add3_u32 v164, s4, v166, v164
	s_add_u32 s0, s0, s14
	s_addc_u32 s1, s1, s15
	s_add_u32 s6, s0, s6
	s_addc_u32 s7, s1, s7
	s_lshl_b64 s[0:1], s[2:3], 2
	s_waitcnt lgkmcnt(0)
	v_mfma_f32_32x32x16_bf16 v[16:31], v[4:7], v[136:139], v[16:31]
	ds_read_b128 v[0:3], v8
	ds_read_b128 v[4:7], v8 offset:256
	v_add_u32_e32 v8, v181, v172
	s_add_u32 s0, s6, s0
	s_addc_u32 s1, s7, s1
	s_mov_b32 s5, 0x10000
	s_waitcnt lgkmcnt(1)
	v_mfma_f32_32x32x16_bf16 v[16:31], v[0:3], v[128:131], v[16:31]
	s_waitcnt lgkmcnt(0)
	v_mfma_f32_32x32x16_bf16 v[16:31], v[4:7], v[132:135], v[16:31]
	v_add_u32_e32 v4, v181, v169
	ds_read_b128 v[0:3], v4
	ds_read_b128 v[4:7], v4 offset:256
	ds_read_b128 v[160:163], v8 offset:256
	s_waitcnt lgkmcnt(2)
	v_mfma_f32_32x32x16_bf16 v[16:31], v[0:3], v[120:123], v[16:31]
	ds_read_b128 v[0:3], v8
	s_waitcnt lgkmcnt(2)
	v_mfma_f32_32x32x16_bf16 v[16:31], v[4:7], v[124:127], v[16:31]
	s_waitcnt lgkmcnt(0)
	v_mfma_f32_32x32x16_bf16 v[16:31], v[0:3], v[112:115], v[16:31]
	ds_read_b128 v[0:3], v204
	ds_read_b128 v[174:177], v204 offset:256
	s_waitcnt lgkmcnt(1)
	v_mfma_f32_32x32x16_bf16 v[0:15], v[0:3], v[152:155], 0
	v_mfma_f32_32x32x16_bf16 v[16:31], v[160:163], v[116:119], v[16:31]
	s_waitcnt lgkmcnt(0)
	v_mfma_f32_32x32x16_bf16 v[0:15], v[174:177], v[156:159], v[0:15]
	v_add_u32_e32 v174, v181, v173
	ds_read_b128 v[160:163], v174
	ds_read_b128 v[176:179], v174 offset:256
	v_xor_b32_e32 v174, 0xe0, v165
	v_add_u32_e32 v175, v181, v174
	v_div_scale_f32 v181, s[8:9], v180, v180, 1.0
	v_rcp_f32_e32 v182, v181
	s_waitcnt lgkmcnt(1)
	v_mfma_f32_32x32x16_bf16 v[16:31], v[160:163], v[108:111], v[16:31]
	v_add_u32_e32 v213, v167, v174
	s_waitcnt lgkmcnt(0)
	v_mfma_f32_32x32x16_bf16 v[16:31], v[176:179], v[104:107], v[16:31]
	ds_read_b128 v[160:163], v175
	ds_read_b128 v[176:179], v175 offset:256
	v_add_u32_e32 v175, v167, v170
	s_waitcnt lgkmcnt(1)
	v_mfma_f32_32x32x16_bf16 v[16:31], v[160:163], v[100:103], v[16:31]
	s_waitcnt lgkmcnt(0)
	v_mfma_f32_32x32x16_bf16 v[16:31], v[176:179], v[96:99], v[16:31]
	ds_read_b128 v[160:163], v175
	ds_read_b128 v[176:179], v175 offset:256
	s_waitcnt lgkmcnt(1)
	v_mfma_f32_32x32x16_bf16 v[0:15], v[160:163], v[148:151], v[0:15]
	ds_read_b128 v[160:163], v207
	s_waitcnt lgkmcnt(1)
	v_mfma_f32_32x32x16_bf16 v[0:15], v[176:179], v[144:147], v[0:15]
	ds_read_b128 v[176:179], v207 offset:256
	s_waitcnt lgkmcnt(1)
	v_mfma_f32_32x32x16_bf16 v[0:15], v[160:163], v[140:143], v[0:15]
	v_fma_f32 v160, -v181, v182, 1.0
	v_fmac_f32_e32 v182, v160, v182
	ds_read_b128 v[160:163], v209
	s_waitcnt lgkmcnt(1)
	v_mfma_f32_32x32x16_bf16 v[0:15], v[176:179], v[136:139], v[0:15]
	v_div_scale_f32 v176, vcc, 1.0, v180, 1.0
	v_mul_f32_e32 v183, v176, v182
	v_fma_f32 v177, -v181, v183, v176
	v_fmac_f32_e32 v183, v177, v182
	v_fma_f32 v181, -v181, v183, v176
	ds_read_b128 v[176:179], v209 offset:256
	s_waitcnt lgkmcnt(1)
	v_mfma_f32_32x32x16_bf16 v[0:15], v[160:163], v[128:131], v[0:15]
	v_div_fmas_f32 v160, v181, v182, v183
	v_div_fixup_f32 v163, v160, v180, 1.0
	ds_read_b128 v[180:183], v210
	v_add3_u32 v162, s4, v184, v185
	v_mul_f32_e32 v16, v163, v16
	s_mov_b32 s4, 0x18000
	s_waitcnt lgkmcnt(1)
	v_mfma_f32_32x32x16_bf16 v[0:15], v[176:179], v[132:135], v[0:15]
	ds_read_b128 v[176:179], v210 offset:256
	ds_read_b128 v[184:187], v211
	ds_read_b128 v[188:191], v211 offset:256
	s_waitcnt lgkmcnt(3)
	v_mfma_f32_32x32x16_bf16 v[0:15], v[180:183], v[120:123], v[0:15]
	ds_read_b128 v[180:183], v212
	ds_read_b128 v[192:195], v212 offset:256
	ds_read_b128 v[196:199], v213
	ds_read_b128 v[200:203], v213 offset:256
	s_waitcnt vmcnt(0)
	s_waitcnt lgkmcnt(0)
	s_barrier
	ds_write_b32 v164, v16
	v_mfma_f32_32x32x16_bf16 v[0:15], v[176:179], v[124:127], v[0:15]
	v_mul_f32_e32 v16, v163, v17
	ds_write_b32 v164, v16 offset:144
	v_mul_f32_e32 v16, v163, v18
	ds_write_b32 v164, v16 offset:288
	v_mul_f32_e32 v16, v163, v19
	ds_write_b32 v164, v16 offset:432
	v_mul_f32_e32 v16, v163, v20
	v_mfma_f32_32x32x16_bf16 v[0:15], v[184:187], v[112:115], v[0:15]
	ds_write_b32 v164, v16 offset:1152
	v_mul_f32_e32 v16, v163, v21
	ds_write_b32 v164, v16 offset:1296
	v_mul_f32_e32 v16, v163, v22
	ds_write_b32 v164, v16 offset:1440
	v_mul_f32_e32 v16, v163, v23
	ds_write_b32 v164, v16 offset:1584
	v_mfma_f32_32x32x16_bf16 v[0:15], v[188:191], v[116:119], v[0:15]
	v_mul_f32_e32 v16, v163, v24
	ds_write_b32 v164, v16 offset:2304
	v_mul_f32_e32 v16, v163, v25
	ds_write_b32 v164, v16 offset:2448
	v_mul_f32_e32 v16, v163, v26
	ds_write_b32 v164, v16 offset:2592
	v_mul_f32_e32 v16, v163, v27
	v_mfma_f32_32x32x16_bf16 v[0:15], v[180:183], v[108:111], v[0:15]
	ds_write_b32 v164, v16 offset:2736
	v_mul_f32_e32 v16, v163, v28
	ds_write_b32 v164, v16 offset:3456
	v_mul_f32_e32 v16, v163, v29
	ds_write_b32 v164, v16 offset:3600
	v_mul_f32_e32 v16, v163, v30
	ds_write_b32 v164, v16 offset:3744
	v_mfma_f32_32x32x16_bf16 v[0:15], v[192:195], v[104:107], v[0:15]
	v_mul_f32_e32 v16, v163, v31
	ds_write_b32 v164, v16 offset:3888
	v_lshl_add_u32 v16, v208, 2, 0
	v_add_u32_e32 v166, 0x22400, v16
	ds_read2_b32 v[192:193], v166 offset1:8
	ds_read_b128 v[176:179], v162
	ds_read_b128 v[180:183], v162 offset:1152
	ds_read2_b32 v[194:195], v166 offset0:16 offset1:24
	ds_read_b128 v[184:187], v162 offset:2304
	ds_read_b128 v[188:191], v162 offset:3456
	v_mfma_f32_32x32x16_bf16 v[0:15], v[196:199], v[100:103], v[0:15]
	v_mfma_f32_32x32x16_bf16 v[0:15], v[200:203], v[96:99], v[0:15]
	s_nop 11
	v_mul_f32_e32 v0, v163, v0
	ds_write_b32 v164, v0
	v_mul_f32_e32 v0, v163, v1
	ds_write_b32 v164, v0 offset:144
	v_mul_f32_e32 v0, v163, v2
	ds_write_b32 v164, v0 offset:288
	v_mul_f32_e32 v0, v163, v3
	ds_write_b32 v164, v0 offset:432
	v_mul_f32_e32 v0, v163, v4
	ds_write_b32 v164, v0 offset:1152
	v_mul_f32_e32 v0, v163, v5
	ds_write_b32 v164, v0 offset:1296
	v_mul_f32_e32 v0, v163, v6
	ds_write_b32 v164, v0 offset:1440
	v_mul_f32_e32 v0, v163, v7
	ds_write_b32 v164, v0 offset:1584
	v_mul_f32_e32 v0, v163, v8
	ds_write_b32 v164, v0 offset:2304
	v_mul_f32_e32 v0, v163, v9
	ds_write_b32 v164, v0 offset:2448
	v_mul_f32_e32 v0, v163, v10
	ds_write_b32 v164, v0 offset:2592
	v_mul_f32_e32 v0, v163, v11
	ds_write_b32 v164, v0 offset:2736
	v_mul_f32_e32 v0, v163, v12
	ds_write_b32 v164, v0 offset:3456
	v_mul_f32_e32 v0, v163, v13
	ds_write_b32 v164, v0 offset:3600
	v_mul_f32_e32 v0, v163, v14
	ds_write_b32 v164, v0 offset:3744
	v_mul_f32_e32 v0, v163, v15
	ds_write_b32 v164, v0 offset:3888
	ds_read_b128 v[0:3], v204 offset:32768
	ds_read_b128 v[4:7], v204 offset:33024
	s_waitcnt lgkmcnt(1)
	v_mfma_f32_32x32x16_bf16 v[16:31], v[0:3], v[152:155], 0
	s_waitcnt lgkmcnt(0)
	v_mfma_f32_32x32x16_bf16 v[16:31], v[4:7], v[156:159], v[16:31]
	ds_read_b128 v[0:3], v175 offset:32768
	ds_read_b128 v[4:7], v175 offset:33024
	s_waitcnt lgkmcnt(1)
	v_mfma_f32_32x32x16_bf16 v[16:31], v[0:3], v[148:151], v[16:31]
	ds_read_b128 v[0:3], v207 offset:32768
	s_waitcnt lgkmcnt(1)
	v_mfma_f32_32x32x16_bf16 v[16:31], v[4:7], v[144:147], v[16:31]
	v_lshlrev_b32_e32 v4, 2, v206
	v_lshl_or_b32 v8, v205, 10, v4
	ds_read_b128 v[4:7], v207 offset:33024
	v_ashrrev_i32_e32 v9, 31, v8
	v_lshl_add_u64 v[160:161], v[8:9], 2, s[0:1]
	s_waitcnt vmcnt(15)
	v_pk_add_f32 v[8:9], v[176:177], v[52:53]
	s_mov_b32 s0, 0x40000
	s_waitcnt lgkmcnt(1)
	v_mfma_f32_32x32x16_bf16 v[16:31], v[0:3], v[140:143], v[16:31]
	ds_read_b128 v[0:3], v209 offset:32768
	s_waitcnt lgkmcnt(1)
	v_mfma_f32_32x32x16_bf16 v[16:31], v[4:7], v[136:139], v[16:31]
	v_add_f32_e64 v4, v178, v54
	v_add_f32_e64 v5, v179, v55
	v_add_f32_e64 v6, v4, v192
	v_add_f32_e64 v7, v5, v192
	v_add_f32_e64 v4, v8, v192
	v_add_f32_e64 v5, v9, v192
	ds_read_b128 v[8:11], v209 offset:33024
	global_store_dwordx4 v[160:161], v[4:7], off nt
	s_waitcnt lgkmcnt(1)
	v_mfma_f32_32x32x16_bf16 v[16:31], v[0:3], v[128:131], v[16:31]
	s_waitcnt vmcnt(15)
	v_add_f32_e64 v0, v182, v62
	v_add_f32_e64 v1, v183, v63
	v_add_f32_e64 v4, v180, v60
	v_add_f32_e64 v5, v181, v61
	v_mov_b32_e32 v6, v193
	v_pk_add_f32 v[2:3], v[0:1], v[6:7] op_sel_hi:[1,0]
	v_pk_add_f32 v[0:1], v[4:5], v[6:7] op_sel_hi:[1,0]
	ds_read_b128 v[4:7], v210 offset:32768
	s_waitcnt lgkmcnt(1)
	v_mfma_f32_32x32x16_bf16 v[16:31], v[8:11], v[132:135], v[16:31]
	v_add_co_u32_e32 v8, vcc, s10, v160
	s_waitcnt vmcnt(14)
	v_add_f32_e64 v10, v184, v76
	v_add_f32_e64 v11, v185, v77
	v_addc_co_u32_e32 v9, vcc, 0, v161, vcc
	global_store_dwordx4 v[8:9], v[0:3], off nt
	ds_read_b128 v[0:3], v210 offset:33024
	s_waitcnt lgkmcnt(1)
	v_mfma_f32_32x32x16_bf16 v[16:31], v[4:7], v[120:123], v[16:31]
	v_add_f32_e64 v8, v186, v78
	v_add_f32_e64 v9, v187, v79
	v_add_f32_e64 v4, v10, v194
	v_add_f32_e64 v5, v11, v194
	v_add_f32_e64 v6, v8, v194
	v_add_f32_e64 v7, v9, v194
	ds_read_b128 v[8:11], v211 offset:32768
	v_add_co_u32_e32 v12, vcc, s5, v160
	v_add_u32_e32 v78, 0x18000, v167
	s_waitcnt lgkmcnt(1)
	v_mfma_f32_32x32x16_bf16 v[16:31], v[0:3], v[124:127], v[16:31]
	v_addc_co_u32_e32 v13, vcc, 0, v161, vcc
	global_store_dwordx4 v[12:13], v[4:7], off nt
	s_waitcnt vmcnt(15)
	v_add_f32_e64 v0, v190, v66
	v_add_f32_e64 v1, v191, v67
	v_add_co_u32_e32 v52, vcc, s4, v160
	v_pk_add_f32 v[4:5], v[188:189], v[64:65]
	v_mov_b32_e32 v6, v195
	v_pk_add_f32 v[2:3], v[0:1], v[6:7] op_sel_hi:[1,0]
	v_pk_add_f32 v[0:1], v[4:5], v[6:7] op_sel_hi:[1,0]
	ds_read_b128 v[4:7], v211 offset:33024
	s_waitcnt lgkmcnt(1)
	v_mfma_f32_32x32x16_bf16 v[16:31], v[8:11], v[112:115], v[16:31]
	ds_read_b128 v[8:11], v162
	ds_read2_b32 v[54:55], v166 offset0:64 offset1:72
	ds_read_b128 v[12:15], v212 offset:32768
	v_addc_co_u32_e32 v53, vcc, 0, v161, vcc
	s_waitcnt vmcnt(14) lgkmcnt(2)
	v_pk_add_f32 v[8:9], v[8:9], v[68:69]
	global_store_dwordx4 v[52:53], v[0:3], off nt
	ds_read_b128 v[0:3], v162 offset:1152
	v_mfma_f32_32x32x16_bf16 v[16:31], v[4:7], v[116:119], v[16:31]
	v_add_f32_e64 v4, v10, v70
	v_add_f32_e64 v5, v11, v71
	s_waitcnt lgkmcnt(2)
	v_add_f32_e64 v6, v4, v54
	v_add_f32_e64 v7, v5, v54
	v_pk_add_f32 v[4:5], v[8:9], v[54:55] op_sel_hi:[1,0]
	ds_read_b128 v[8:11], v212 offset:33024
	s_waitcnt vmcnt(14) lgkmcnt(1)
	v_pk_add_f32 v[2:3], v[2:3], v[74:75]
	v_pk_add_f32 v[0:1], v[0:1], v[72:73]
	v_mfma_f32_32x32x16_bf16 v[16:31], v[12:15], v[108:111], v[16:31]
	v_add_co_u32_e32 v12, vcc, s0, v160
	s_mov_b32 s0, 0x48000
	s_nop 0
	v_addc_co_u32_e32 v13, vcc, 0, v161, vcc
	global_store_dwordx4 v[12:13], v[4:7], off nt
	ds_read_b128 v[4:7], v213 offset:32768
	s_waitcnt lgkmcnt(1)
	v_mfma_f32_32x32x16_bf16 v[16:31], v[8:11], v[104:107], v[16:31]
	v_mov_b32_e32 v8, v55
	v_add_f32_e64 v2, v2, v8
	v_add_f32_e64 v3, v3, v8
	v_add_f32_e64 v0, v0, v8
	v_add_f32_e64 v1, v1, v8
	ds_read_b128 v[8:11], v213 offset:33024
	v_add_u32_e32 v12, v78, v165
	s_waitcnt lgkmcnt(1)
	v_mfma_f32_32x32x16_bf16 v[16:31], v[4:7], v[100:103], v[16:31]
	v_add_co_u32_e32 v4, vcc, s0, v160
	s_mov_b32 s0, 0x50000
	s_nop 0
	v_addc_co_u32_e32 v5, vcc, 0, v161, vcc
	global_store_dwordx4 v[4:5], v[0:3], off nt
	ds_read_b128 v[0:3], v162 offset:2304
	ds_read2_b32 v[64:65], v166 offset0:80 offset1:88
	ds_read_b128 v[4:7], v12
	ds_read_b128 v[60:63], v12 offset:256
	s_waitcnt lgkmcnt(4)
	v_mfma_f32_32x32x16_bf16 v[16:31], v[8:11], v[96:99], v[16:31]
	s_waitcnt vmcnt(15) lgkmcnt(3)
	v_add_f32_e64 v2, v2, v58
	v_add_f32_e64 v3, v3, v59
	v_add_f32_e64 v0, v0, v56
	v_add_f32_e64 v1, v1, v57
	s_waitcnt lgkmcnt(2)
	v_pk_add_f32 v[58:59], v[2:3], v[64:65] op_sel_hi:[1,0]
	v_pk_add_f32 v[56:57], v[0:1], v[64:65] op_sel_hi:[1,0]
	ds_read_b128 v[52:55], v162 offset:3456
	v_add_co_u32_e32 v66, vcc, s0, v160
	s_waitcnt lgkmcnt(2)
	v_mfma_f32_32x32x16_bf16 v[0:15], v[4:7], v[152:155], 0
	v_addc_co_u32_e32 v67, vcc, 0, v161, vcc
	global_store_dwordx4 v[66:67], v[56:59], off nt
	s_waitcnt vmcnt(15) lgkmcnt(0)
	v_add_f32_e64 v50, v54, v50
	v_add_f32_e64 v51, v55, v51
	v_pk_add_f32 v[48:49], v[52:53], v[48:49]
	v_add_u32_e32 v58, v78, v170
	ds_read_b128 v[54:57], v58
	v_mfma_f32_32x32x16_bf16 v[0:15], v[60:63], v[156:159], v[0:15]
	ds_read_b128 v[58:61], v58 offset:256
	v_mov_b32_e32 v52, v65
	v_add_u32_e32 v62, v78, v168
	v_add_f32_e64 v50, v50, v52
	v_add_f32_e64 v51, v51, v52
	v_pk_add_f32 v[48:49], v[48:49], v[52:53] op_sel_hi:[1,0]
	v_mul_f32_e32 v16, v163, v16
	s_mov_b32 s0, 0x58000
	s_waitcnt lgkmcnt(1)
	v_mfma_f32_32x32x16_bf16 v[0:15], v[54:57], v[148:151], v[0:15]
	ds_read_b128 v[52:55], v62
	ds_read_b128 v[62:65], v62 offset:256
	v_add_u32_e32 v56, v78, v171
	ds_read_b128 v[66:69], v56
	ds_read_b128 v[70:73], v56 offset:256
	v_add_u32_e32 v56, v78, v169
	ds_read_b128 v[74:77], v56
	ds_read_b128 v[148:151], v56 offset:256
	s_waitcnt lgkmcnt(6)
	v_mfma_f32_32x32x16_bf16 v[0:15], v[58:61], v[144:147], v[0:15]
	v_add_u32_e32 v60, v78, v172
	ds_read_b128 v[56:59], v60
	ds_read_b128 v[144:147], v60 offset:256
	v_add_u32_e32 v60, v78, v173
	ds_read_b128 v[152:155], v60
	ds_read_b128 v[156:159], v60 offset:256
	v_add_u32_e32 v60, v78, v174
	s_waitcnt lgkmcnt(9)
	v_mfma_f32_32x32x16_bf16 v[0:15], v[52:55], v[140:143], v[0:15]
	ds_read_b128 v[52:55], v60
	ds_read_b128 v[140:143], v60 offset:256
	ds_write_b32 v164, v16
	v_mul_f32_e32 v16, v163, v17
	ds_write_b32 v164, v16 offset:144
	v_mul_f32_e32 v16, v163, v18
	ds_write_b32 v164, v16 offset:288
	v_mul_f32_e32 v16, v163, v19
	s_waitcnt lgkmcnt(13)
	v_mfma_f32_32x32x16_bf16 v[0:15], v[62:65], v[136:139], v[0:15]
	ds_write_b32 v164, v16 offset:432
	v_mul_f32_e32 v16, v163, v20
	ds_write_b32 v164, v16 offset:1152
	v_mul_f32_e32 v16, v163, v21
	ds_write_b32 v164, v16 offset:1296
	v_mul_f32_e32 v16, v163, v22
	ds_write_b32 v164, v16 offset:1440
	s_waitcnt lgkmcnt(14)
	v_mfma_f32_32x32x16_bf16 v[0:15], v[66:69], v[128:131], v[0:15]
	v_mul_f32_e32 v16, v163, v23
	ds_write_b32 v164, v16 offset:1584
	v_mul_f32_e32 v16, v163, v24
	ds_write_b32 v164, v16 offset:2304
	v_mul_f32_e32 v16, v163, v25
	ds_write_b32 v164, v16 offset:2448
	v_mul_f32_e32 v16, v163, v26
	v_mfma_f32_32x32x16_bf16 v[0:15], v[70:73], v[132:135], v[0:15]
	ds_write_b32 v164, v16 offset:2592
	v_mul_f32_e32 v16, v163, v27
	ds_write_b32 v164, v16 offset:2736
	v_mul_f32_e32 v16, v163, v28
	ds_write_b32 v164, v16 offset:3456
	v_mul_f32_e32 v16, v163, v29
	ds_write_b32 v164, v16 offset:3600
	v_mfma_f32_32x32x16_bf16 v[0:15], v[74:77], v[120:123], v[0:15]
	v_mul_f32_e32 v16, v163, v30
	ds_write_b32 v164, v16 offset:3744
	v_mul_f32_e32 v16, v163, v31
	ds_write_b32 v164, v16 offset:3888
	ds_read_b128 v[16:19], v162
	v_add_co_u32_e32 v20, vcc, s0, v160
	s_waitcnt lgkmcnt(14)
	v_mfma_f32_32x32x16_bf16 v[0:15], v[148:151], v[124:127], v[0:15]
	v_addc_co_u32_e32 v21, vcc, 0, v161, vcc
	ds_read2_b32 v[24:25], v166 offset0:128 offset1:136
	global_store_dwordx4 v[20:21], v[48:51], off nt
	ds_read_b128 v[20:23], v162 offset:1152
	s_mov_b32 s0, 0x80000
	s_waitcnt vmcnt(15) lgkmcnt(2)
	v_pk_add_f32 v[18:19], v[18:19], v[90:91]
	v_mfma_f32_32x32x16_bf16 v[0:15], v[56:59], v[112:115], v[0:15]
	v_add_f32_e64 v16, v16, v88
	v_add_f32_e64 v17, v17, v89
	v_add_co_u32_e32 v26, vcc, s0, v160
	s_waitcnt lgkmcnt(1)
	v_add_f32_e64 v18, v18, v24
	v_add_f32_e64 v19, v19, v24
	v_pk_add_f32 v[16:17], v[16:17], v[24:25] op_sel_hi:[1,0]
	v_addc_co_u32_e32 v27, vcc, 0, v161, vcc
	v_mfma_f32_32x32x16_bf16 v[0:15], v[144:147], v[116:119], v[0:15]
	s_mov_b32 s0, 0x88000
	global_store_dwordx4 v[26:27], v[16:19], off nt
	s_waitcnt vmcnt(15) lgkmcnt(0)
	v_add_f32_e64 v20, v20, v92
	v_add_f32_e64 v21, v21, v93
	v_add_co_u32_e32 v24, vcc, s0, v160
	v_pk_add_f32 v[16:17], v[22:23], v[94:95]
	v_mov_b32_e32 v22, v25
	v_mfma_f32_32x32x16_bf16 v[0:15], v[152:155], v[108:111], v[0:15]
	v_add_f32_e64 v18, v16, v22
	v_add_f32_e64 v19, v17, v22
	v_add_f32_e64 v16, v20, v22
	v_add_f32_e64 v17, v21, v22
	v_addc_co_u32_e32 v25, vcc, 0, v161, vcc
	global_store_dwordx4 v[24:25], v[16:19], off nt
	ds_read_b128 v[20:23], v162 offset:2304
	ds_read2_b32 v[24:25], v166 offset0:144 offset1:152
	ds_read_b128 v[16:19], v162 offset:3456
	v_mfma_f32_32x32x16_bf16 v[0:15], v[156:159], v[104:107], v[0:15]
	s_mov_b32 s0, 0x90000
	v_add_co_u32_e32 v26, vcc, s0, v160
	s_waitcnt vmcnt(15) lgkmcnt(2)
	v_add_f32_e64 v22, v22, v82
	v_add_f32_e64 v23, v23, v83
	v_pk_add_f32 v[20:21], v[20:21], v[80:81]
	s_waitcnt lgkmcnt(1)
	v_pk_add_f32 v[22:23], v[22:23], v[24:25] op_sel_hi:[1,0]
	v_pk_add_f32 v[20:21], v[20:21], v[24:25] op_sel_hi:[1,0]
	v_mfma_f32_32x32x16_bf16 v[0:15], v[52:55], v[100:103], v[0:15]
	v_addc_co_u32_e32 v27, vcc, 0, v161, vcc
	s_mov_b32 s0, 0x98000
	global_store_dwordx4 v[26:27], v[20:23], off nt
	s_waitcnt vmcnt(15) lgkmcnt(0)
	v_add_f32_e64 v18, v18, v86
	v_add_f32_e64 v19, v19, v87
	v_pk_add_f32 v[16:17], v[16:17], v[84:85]
	v_mov_b32_e32 v20, v25
	v_mfma_f32_32x32x16_bf16 v[0:15], v[140:143], v[96:99], v[0:15]
	v_add_f32_e64 v18, v18, v20
	v_add_f32_e64 v19, v19, v20
	v_add_f32_e64 v16, v16, v20
	v_add_f32_e64 v17, v17, v20
	s_nop 7
	v_mul_f32_e32 v0, v163, v0
	ds_write_b32 v164, v0
	v_mul_f32_e32 v0, v163, v1
	ds_write_b32 v164, v0 offset:144
	v_mul_f32_e32 v0, v163, v2
	ds_write_b32 v164, v0 offset:288
	v_mul_f32_e32 v0, v163, v3
	ds_write_b32 v164, v0 offset:432
	v_mul_f32_e32 v0, v163, v4
	ds_write_b32 v164, v0 offset:1152
	v_mul_f32_e32 v0, v163, v5
	ds_write_b32 v164, v0 offset:1296
	v_mul_f32_e32 v0, v163, v6
	ds_write_b32 v164, v0 offset:1440
	v_mul_f32_e32 v0, v163, v7
	ds_write_b32 v164, v0 offset:1584
	v_mul_f32_e32 v0, v163, v8
	ds_write_b32 v164, v0 offset:2304
	v_mul_f32_e32 v0, v163, v9
	ds_write_b32 v164, v0 offset:2448
	v_mul_f32_e32 v0, v163, v10
	ds_write_b32 v164, v0 offset:2592
	v_mul_f32_e32 v0, v163, v11
	ds_write_b32 v164, v0 offset:2736
	v_mul_f32_e32 v0, v163, v12
	ds_write_b32 v164, v0 offset:3456
	v_mul_f32_e32 v0, v163, v13
	ds_write_b32 v164, v0 offset:3600
	v_mul_f32_e32 v0, v163, v14
	ds_write_b32 v164, v0 offset:3744
	v_mul_f32_e32 v0, v163, v15
	ds_write_b32 v164, v0 offset:3888
	ds_read_b128 v[0:3], v162
	v_add_co_u32_e32 v4, vcc, s0, v160
	ds_read2_b32 v[8:9], v166 offset0:192 offset1:200
	s_nop 0
	v_addc_co_u32_e32 v5, vcc, 0, v161, vcc
	global_store_dwordx4 v[4:5], v[16:19], off nt
	ds_read_b128 v[4:7], v162 offset:1152
	s_mov_b32 s0, 0xc0000
	s_waitcnt vmcnt(15) lgkmcnt(2)
	v_pk_add_f32 v[2:3], v[2:3], v[42:43]
	v_pk_add_f32 v[0:1], v[0:1], v[40:41]
	v_add_co_u32_e32 v10, vcc, s0, v160
	s_waitcnt lgkmcnt(1)
	v_pk_add_f32 v[2:3], v[2:3], v[8:9] op_sel_hi:[1,0]
	v_pk_add_f32 v[0:1], v[0:1], v[8:9] op_sel_hi:[1,0]
	v_addc_co_u32_e32 v11, vcc, 0, v161, vcc
	global_store_dwordx4 v[10:11], v[0:3], off nt
	s_waitcnt vmcnt(15) lgkmcnt(0)
	v_pk_add_f32 v[4:5], v[4:5], v[44:45]
	s_mov_b32 s0, 0xc8000
	v_pk_add_f32 v[0:1], v[6:7], v[46:47]
	v_mov_b32_e32 v6, v9
	v_pk_add_f32 v[2:3], v[0:1], v[6:7] op_sel_hi:[1,0]
	v_pk_add_f32 v[0:1], v[4:5], v[6:7] op_sel_hi:[1,0]
	ds_read_b128 v[4:7], v162 offset:2304
	v_add_co_u32_e32 v8, vcc, s0, v160
	ds_read2_b32 v[10:11], v166 offset0:208 offset1:216
	s_nop 0
	v_addc_co_u32_e32 v9, vcc, 0, v161, vcc
	global_store_dwordx4 v[8:9], v[0:3], off nt
	ds_read_b128 v[0:3], v162 offset:3456
	s_mov_b32 s0, 0xd0000
	s_waitcnt vmcnt(15) lgkmcnt(2)
	v_pk_add_f32 v[6:7], v[6:7], v[34:35]
	v_pk_add_f32 v[4:5], v[4:5], v[32:33]
	v_add_co_u32_e32 v8, vcc, s0, v160
	s_waitcnt lgkmcnt(1)
	v_pk_add_f32 v[6:7], v[6:7], v[10:11] op_sel_hi:[1,0]
	v_pk_add_f32 v[4:5], v[4:5], v[10:11] op_sel_hi:[1,0]
	v_addc_co_u32_e32 v9, vcc, 0, v161, vcc
	global_store_dwordx4 v[8:9], v[4:7], off nt
	s_waitcnt vmcnt(15) lgkmcnt(0)
	v_pk_add_f32 v[2:3], v[2:3], v[38:39]
	v_pk_add_f32 v[0:1], v[0:1], v[36:37]
	v_mov_b32_e32 v4, v11
	v_pk_add_f32 v[2:3], v[2:3], v[4:5] op_sel_hi:[1,0]
	v_pk_add_f32 v[0:1], v[0:1], v[4:5] op_sel_hi:[1,0]
	v_add_co_u32_e32 v4, vcc, 0xd8000, v160
	s_nop 1
	v_addc_co_u32_e32 v5, vcc, 0, v161, vcc
	global_store_dwordx4 v[4:5], v[0:3], off nt
	s_endpgm
